# batch 3 plus non-temporal stores for the expert output slots (yslot) written by M2
# speedup vs baseline: 1.0615x; 1.0478x over previous
; #define LAS __attribute__((address_space(3)))
;     DI void operator()(const f32x4 (&acc)[2][2][4][2], const Unit& u, int wr, int wc, int fr, int fq) const {
;         int lrow = 64 * wr + fr, cwl = 32 * wc + 8 * fq; asm volatile("" : "+v"(lrow), "+v"(cwl));
;         const int n = u.n; const int cw = u.pn * 256 + cwl;
;         const char* lb = (const char*)lists + (size_t)u.e * LIST_CAP * 8;
;         f32x4 bv[2][2];
; #pragma unroll
;         for (int bj = 0; bj < 2; ++bj) { const LAS float* bb = bl + cwl + bj * 128; bv[bj][0] = *(const LAS f32x4*)bb; bv[bj][1] = *(const LAS f32x4*)(bb + 4); }
;         constexpr float dq = 1.0f / (W8_SCALE * ACT8_SCALE);
; #pragma unroll
;         for (int ai = 0; ai < 2; ++ai) { if (u.half == 2 - ai) continue;
;             const bool oddq = (fq & 1) != 0;
; #pragma unroll
;             for (int p2 = 0; p2 < 2; ++p2) { u32x2 wq[2][2];
;                 const u32x2 en0 = *(const LAS u32x2*)((const LAS unsigned char*)entl + (128 * ai + 32 * p2 + lrow) * 8), en1 = *(const LAS u32x2*)((const LAS unsigned char*)entl + (128 * ai + 32 * p2 + 16 + lrow) * 8);
; #pragma unroll
;                 for (int r2 = 0; r2 < 2; ++r2) { const int m = 2 * p2 + r2; const float gs = __uint_as_float(r2 ? en1.y : en0.y) * YS8_SCALE;
;                     const f32x4 a0 = (acc[ai][0][m][0] * dq + bv[0][0]) * gs, a1 = (acc[ai][0][m][1] * dq + bv[0][1]) * gs, b0 = (acc[ai][1][m][0] * dq + bv[1][0]) * gs, b1 = (acc[ai][1][m][1] * dq + bv[1][1]) * gs;
;                     wq[r2][0].x = pk4_fp8(a0[0], a0[1], a0[2], a0[3]); wq[r2][0].y = pk4_fp8(a1[0], a1[1], a1[2], a1[3]); wq[r2][1].x = pk4_fp8(b0[0], b0[1], b0[2], b0[3]); wq[r2][1].y = pk4_fp8(b1[0], b1[1], b1[2], b1[3]); }
;                 const int msel = 2 * p2 + (oddq ? 1 : 0); const int li = u.j * 256 + 128 * ai + 16 * msel + lrow;
;                 char* dst = (char*)yslot + ((oddq ? en1.x : en0.x) * (unsigned)D + (unsigned)(cw - (oddq ? 8 : 0)));
; #pragma unroll
;                 for (int bj = 0; bj < 2; ++bj) { const auto rx = __builtin_amdgcn_permlane16_swap(wq[0][bj].x, wq[1][bj].x, false, false), ry = __builtin_amdgcn_permlane16_swap(wq[0][bj].y, wq[1][bj].y, false, false);
;                     u32x4 w; w.x = rx[0]; w.y = ry[0]; w.z = rx[1]; w.w = ry[1];
;                     if (li < n) *(u32x4*)(dst + 128 * bj) = w; } }
.LBB0_1328:
	s_mov_b32 s0, s39
	s_mov_b32 s1, -1
	s_and_b64 vcc, exec, s[4:5]
	v_mbcnt_lo_u32_b32 v0, s1, 0
	v_mbcnt_hi_u32_b32 v0, s1, v0
	s_lshl_b32 s1, s0, 4
	s_lshl_b32 s0, s0, 5
	s_andn2_b32 s1, s1, 63
	v_ashrrev_i32_e32 v18, 4, v0
	s_and_b32 s0, s0, 0x60
	v_and_or_b32 v0, v0, 15, s1
	v_lshl_add_u32 v19, v18, 3, s0
	v_and_b32_e32 v18, 1, v18
	v_lshl_add_u32 v2, v19, 2, 0
	v_add_u32_e32 v2, 0x21000, v2
	ds_read_b128 v[14:17], v2
	ds_read_b128 v[10:13], v2 offset:16
	ds_read_b128 v[6:9], v2 offset:512
	ds_read_b128 v[2:5], v2 offset:528
	v_add_u32_e32 v19, s2, v19
	v_cmp_eq_u32_e64 s[6:7], 0, v18
	v_lshl_add_u32 v31, v18, 4, v0
	v_lshlrev_b32_e32 v18, 3, v18
	v_sub_u32_e32 v28, v19, v18
	v_lshlrev_b32_e32 v30, 3, v0
	s_mov_b64 s[2:3], -1
	v_add_u32_e32 v29, s17, v31
	v_readlane_b32 s72, v253, 25
	v_readlane_b32 s73, v253, 26
	s_cbranch_vccnz .LBB0_1339
	v_add_u32_e32 v0, 0, v30
	v_add_u32_e32 v0, 0x20700, v0
	s_waitcnt lgkmcnt(0)
	ds_read2_b64 v[32:35], v0 offset1:16
	v_pk_fma_f32 v[18:19], v[192:193], s[50:51], v[16:17] op_sel_hi:[1,0,1]
	v_pk_fma_f32 v[20:21], v[190:191], s[50:51], v[14:15] op_sel_hi:[1,0,1]
	v_pk_fma_f32 v[22:23], v[188:189], s[50:51], v[12:13] op_sel_hi:[1,0,1]
	v_pk_fma_f32 v[38:39], v[178:179], s[50:51], v[10:11] op_sel_hi:[1,0,1]
	s_waitcnt lgkmcnt(0)
	v_mul_f32_e32 v26, 0x42800000, v33
	v_pk_mul_f32 v[24:25], v[18:19], v[26:27] op_sel_hi:[1,0]
	v_pk_mul_f32 v[18:19], v[20:21], v[26:27] op_sel_hi:[1,0]
	v_pk_fma_f32 v[20:21], v[186:187], s[50:51], v[10:11] op_sel_hi:[1,0,1]
	v_med3_f32 v0, v18, s53, v204
	v_pk_mul_f32 v[20:21], v[20:21], v[26:27] op_sel_hi:[1,0]
	v_med3_f32 v19, v19, s53, v204
	v_mov_b32_e32 v18, v1
	v_cvt_pk_fp8_f32 v18, v0, v19
	v_med3_f32 v20, v20, s53, v204
	v_med3_f32 v21, v21, s53, v204
	v_mov_b32_e32 v19, v1
	v_cvt_pk_fp8_f32 v19, v20, v21
	v_pk_mul_f32 v[22:23], v[22:23], v[26:27] op_sel_hi:[1,0]
	v_med3_f32 v0, v24, s53, v204
	v_med3_f32 v24, v25, s53, v204
	v_cvt_pk_fp8_f32 v18, v0, v24 op_sel:[0,0,1]
	v_med3_f32 v0, v22, s53, v204
	v_med3_f32 v20, v23, s53, v204
	v_cvt_pk_fp8_f32 v19, v0, v20 op_sel:[0,0,1]
	v_mul_f32_e32 v22, 0x42800000, v35
	v_pk_fma_f32 v[20:21], v[184:185], s[50:51], v[16:17] op_sel_hi:[1,0,1]
	v_pk_fma_f32 v[24:25], v[182:183], s[50:51], v[14:15] op_sel_hi:[1,0,1]
	v_pk_mul_f32 v[36:37], v[20:21], v[22:23] op_sel_hi:[1,0]
	v_pk_mul_f32 v[20:21], v[24:25], v[22:23] op_sel_hi:[1,0]
	v_pk_mul_f32 v[38:39], v[38:39], v[22:23] op_sel_hi:[1,0]
	v_med3_f32 v0, v20, s53, v204
	v_med3_f32 v21, v21, s53, v204
	v_mov_b32_e32 v20, v1
	v_cvt_pk_fp8_f32 v20, v0, v21
	v_med3_f32 v27, v38, s53, v204
	v_med3_f32 v33, v39, s53, v204
	v_mov_b32_e32 v21, v1
	v_cvt_pk_fp8_f32 v21, v27, v33
	v_pk_fma_f32 v[24:25], v[180:181], s[50:51], v[12:13] op_sel_hi:[1,0,1]
	v_med3_f32 v0, v36, s53, v204
	v_pk_mul_f32 v[24:25], v[24:25], v[22:23] op_sel_hi:[1,0]
	v_med3_f32 v23, v37, s53, v204
	v_cvt_pk_fp8_f32 v20, v0, v23 op_sel:[0,0,1]
	v_med3_f32 v0, v24, s53, v204
	v_med3_f32 v23, v25, s53, v204
	v_cvt_pk_fp8_f32 v21, v0, v23 op_sel:[0,0,1]
	v_cndmask_b32_e64 v0, v34, v32, s[6:7]
	v_lshl_add_u32 v0, v0, 10, v28
	v_lshl_add_u64 v[24:25], s[10:11], 0, v[0:1]
	v_cmp_gt_i32_e32 vcc, s70, v29
	v_permlane16_swap_b32_e32 v18, v20
	v_permlane16_swap_b32_e32 v19, v21
	s_and_saveexec_b64 s[2:3], vcc
	s_cbranch_execz .LBB0_1331
	global_store_dwordx4 v[24:25], v[18:21], off nt
.LBB0_1331:
	s_or_b64 exec, exec, s[2:3]
	v_mov_b32_e32 v27, v26
	v_pk_fma_f32 v[18:19], v[176:177], s[50:51], v[8:9] op_sel_hi:[1,0,1]
	v_pk_fma_f32 v[20:21], v[174:175], s[50:51], v[6:7] op_sel_hi:[1,0,1]
	v_mov_b32_e32 v32, v26
	v_mov_b32_e32 v33, v26
	v_pk_mul_f32 v[34:35], v[18:19], v[32:33]
	v_pk_mul_f32 v[18:19], v[20:21], v[26:27]
	v_pk_fma_f32 v[36:37], v[170:171], s[50:51], v[2:3] op_sel_hi:[1,0,1]
	v_med3_f32 v0, v18, s53, v204
	v_pk_mul_f32 v[26:27], v[36:37], v[26:27]
	v_med3_f32 v19, v19, s53, v204
	v_mov_b32_e32 v18, v1
	v_cvt_pk_fp8_f32 v18, v0, v19
	v_med3_f32 v26, v26, s53, v204
	v_med3_f32 v27, v27, s53, v204
	v_mov_b32_e32 v19, v1
	v_cvt_pk_fp8_f32 v19, v26, v27
	v_pk_fma_f32 v[20:21], v[172:173], s[50:51], v[4:5] op_sel_hi:[1,0,1]
	v_med3_f32 v0, v34, s53, v204
	v_pk_mul_f32 v[20:21], v[20:21], v[32:33]
	v_med3_f32 v32, v35, s53, v204
	v_cvt_pk_fp8_f32 v18, v0, v32 op_sel:[0,0,1]
	v_med3_f32 v0, v20, s53, v204
	v_med3_f32 v20, v21, s53, v204
	v_mov_b32_e32 v23, v22
	v_cvt_pk_fp8_f32 v19, v0, v20 op_sel:[0,0,1]
	v_pk_fma_f32 v[20:21], v[168:169], s[50:51], v[8:9] op_sel_hi:[1,0,1]
	v_pk_fma_f32 v[26:27], v[166:167], s[50:51], v[6:7] op_sel_hi:[1,0,1]
	v_mov_b32_e32 v32, v22
	v_mov_b32_e32 v33, v22
	v_pk_mul_f32 v[34:35], v[20:21], v[32:33]
	v_pk_mul_f32 v[20:21], v[26:27], v[22:23]
	v_pk_fma_f32 v[36:37], v[162:163], s[50:51], v[2:3] op_sel_hi:[1,0,1]
	v_med3_f32 v0, v20, s53, v204
	v_pk_mul_f32 v[22:23], v[36:37], v[22:23]
	v_med3_f32 v21, v21, s53, v204
	v_mov_b32_e32 v20, v1
	v_cvt_pk_fp8_f32 v20, v0, v21
	v_med3_f32 v22, v22, s53, v204
	v_med3_f32 v23, v23, s53, v204
	v_mov_b32_e32 v21, v1
	v_cvt_pk_fp8_f32 v21, v22, v23
	v_pk_fma_f32 v[26:27], v[164:165], s[50:51], v[4:5] op_sel_hi:[1,0,1]
	v_med3_f32 v0, v34, s53, v204
	v_pk_mul_f32 v[26:27], v[26:27], v[32:33]
	v_med3_f32 v32, v35, s53, v204
	v_cvt_pk_fp8_f32 v20, v0, v32 op_sel:[0,0,1]
	v_med3_f32 v0, v26, s53, v204
	v_med3_f32 v22, v27, s53, v204
	v_cvt_pk_fp8_f32 v21, v0, v22 op_sel:[0,0,1]
	v_permlane16_swap_b32_e32 v18, v20
	s_nop 0
	v_permlane16_swap_b32_e32 v19, v21
	s_and_saveexec_b64 s[2:3], vcc
	s_cbranch_execz .LBB0_1333
	global_store_dwordx4 v[24:25], v[18:21], off offset:128 nt
; #define LAS __attribute__((address_space(3)))
; DI unsigned pk4_fp8(float a, float b, float c, float d) { int r = 0; r = __builtin_amdgcn_cvt_pk_fp8_f32(sat8(a), sat8(b), r, false); r = __builtin_amdgcn_cvt_pk_fp8_f32(sat8(c), sat8(d), r, true); return (unsigned)r; }
;     DI void operator()(const f32x4 (&acc)[2][2][4][2], const Unit& u, int wr, int wc, int fr, int fq) const {
;     ...
;         for (int ai = 0; ai < 2; ++ai) { if (u.half == 2 - ai) continue;
;             const bool oddq = (fq & 1) != 0;
; #pragma unroll
;             for (int p2 = 0; p2 < 2; ++p2) { u32x2 wq[2][2];
;                 const u32x2 en0 = *(const LAS u32x2*)((const LAS unsigned char*)entl + (128 * ai + 32 * p2 + lrow) * 8), en1 = *(const LAS u32x2*)((const LAS unsigned char*)entl + (128 * ai + 32 * p2 + 16 + lrow) * 8);
; #pragma unroll
;                 for (int r2 = 0; r2 < 2; ++r2) { const int m = 2 * p2 + r2; const float gs = __uint_as_float(r2 ? en1.y : en0.y) * YS8_SCALE;
;                     const f32x4 a0 = (acc[ai][0][m][0] * dq + bv[0][0]) * gs, a1 = (acc[ai][0][m][1] * dq + bv[0][1]) * gs, b0 = (acc[ai][1][m][0] * dq + bv[1][0]) * gs, b1 = (acc[ai][1][m][1] * dq + bv[1][1]) * gs;
;                     wq[r2][0].x = pk4_fp8(a0[0], a0[1], a0[2], a0[3]); wq[r2][0].y = pk4_fp8(a1[0], a1[1], a1[2], a1[3]); wq[r2][1].x = pk4_fp8(b0[0], b0[1], b0[2], b0[3]); wq[r2][1].y = pk4_fp8(b1[0], b1[1], b1[2], b1[3]); }
;                 const int msel = 2 * p2 + (oddq ? 1 : 0); const int li = u.j * 256 + 128 * ai + 16 * msel + lrow;
;                 char* dst = (char*)yslot + ((oddq ? en1.x : en0.x) * (unsigned)D + (unsigned)(cw - (oddq ? 8 : 0)));
; #pragma unroll
;                 for (int bj = 0; bj < 2; ++bj) { const auto rx = __builtin_amdgcn_permlane16_swap(wq[0][bj].x, wq[1][bj].x, false, false), ry = __builtin_amdgcn_permlane16_swap(wq[0][bj].y, wq[1][bj].y, false, false);
;                     u32x4 w; w.x = rx[0]; w.y = ry[0]; w.z = rx[1]; w.w = ry[1];
;                     if (li < n) *(u32x4*)(dst + 128 * bj) = w; } }
.LBB0_1333:
	s_or_b64 exec, exec, s[2:3]
	s_add_i32 s0, 0, 0x20700
	v_add_u32_e32 v0, s0, v30
	ds_read2_b64 v[32:35], v0 offset0:32 offset1:48
	v_pk_fma_f32 v[18:19], v[160:161], s[50:51], v[16:17] op_sel_hi:[1,0,1]
	v_pk_fma_f32 v[20:21], v[158:159], s[50:51], v[14:15] op_sel_hi:[1,0,1]
	v_pk_fma_f32 v[22:23], v[156:157], s[50:51], v[12:13] op_sel_hi:[1,0,1]
	v_pk_fma_f32 v[38:39], v[146:147], s[50:51], v[10:11] op_sel_hi:[1,0,1]
	s_waitcnt lgkmcnt(0)
	v_mul_f32_e32 v26, 0x42800000, v33
	v_pk_mul_f32 v[24:25], v[18:19], v[26:27] op_sel_hi:[1,0]
	v_pk_mul_f32 v[18:19], v[20:21], v[26:27] op_sel_hi:[1,0]
	v_pk_fma_f32 v[20:21], v[154:155], s[50:51], v[10:11] op_sel_hi:[1,0,1]
	v_med3_f32 v0, v18, s53, v204
	v_pk_mul_f32 v[20:21], v[20:21], v[26:27] op_sel_hi:[1,0]
	v_med3_f32 v19, v19, s53, v204
	v_mov_b32_e32 v18, v1
	v_cvt_pk_fp8_f32 v18, v0, v19
	v_med3_f32 v20, v20, s53, v204
	v_med3_f32 v21, v21, s53, v204
	v_mov_b32_e32 v19, v1
	v_cvt_pk_fp8_f32 v19, v20, v21
	v_pk_mul_f32 v[22:23], v[22:23], v[26:27] op_sel_hi:[1,0]
	v_med3_f32 v0, v24, s53, v204
	v_med3_f32 v24, v25, s53, v204
	v_cvt_pk_fp8_f32 v18, v0, v24 op_sel:[0,0,1]
	v_med3_f32 v0, v22, s53, v204
	v_med3_f32 v20, v23, s53, v204
	v_cvt_pk_fp8_f32 v19, v0, v20 op_sel:[0,0,1]
	v_mul_f32_e32 v22, 0x42800000, v35
	v_pk_fma_f32 v[20:21], v[152:153], s[50:51], v[16:17] op_sel_hi:[1,0,1]
	v_pk_fma_f32 v[24:25], v[150:151], s[50:51], v[14:15] op_sel_hi:[1,0,1]
	v_pk_mul_f32 v[36:37], v[20:21], v[22:23] op_sel_hi:[1,0]
	v_pk_mul_f32 v[20:21], v[24:25], v[22:23] op_sel_hi:[1,0]
	v_pk_mul_f32 v[38:39], v[38:39], v[22:23] op_sel_hi:[1,0]
	v_med3_f32 v0, v20, s53, v204
	v_med3_f32 v21, v21, s53, v204
	v_mov_b32_e32 v20, v1
	v_cvt_pk_fp8_f32 v20, v0, v21
	v_med3_f32 v27, v38, s53, v204
	v_med3_f32 v33, v39, s53, v204
	v_mov_b32_e32 v21, v1
	v_cvt_pk_fp8_f32 v21, v27, v33
	v_pk_fma_f32 v[24:25], v[148:149], s[50:51], v[12:13] op_sel_hi:[1,0,1]
	v_med3_f32 v0, v36, s53, v204
	v_pk_mul_f32 v[24:25], v[24:25], v[22:23] op_sel_hi:[1,0]
	v_med3_f32 v23, v37, s53, v204
	v_cvt_pk_fp8_f32 v20, v0, v23 op_sel:[0,0,1]
	v_med3_f32 v0, v24, s53, v204
	v_med3_f32 v23, v25, s53, v204
	v_cvt_pk_fp8_f32 v21, v0, v23 op_sel:[0,0,1]
	v_cndmask_b32_e64 v0, v34, v32, s[6:7]
	v_add3_u32 v23, v31, s17, 32
	v_lshl_add_u32 v0, v0, 10, v28
	v_lshl_add_u64 v[24:25], s[10:11], 0, v[0:1]
	v_cmp_gt_i32_e32 vcc, s70, v23
	v_permlane16_swap_b32_e32 v18, v20
	v_permlane16_swap_b32_e32 v19, v21
	s_and_saveexec_b64 s[2:3], vcc
	s_cbranch_execz .LBB0_1335
	global_store_dwordx4 v[24:25], v[18:21], off nt
.LBB0_1335:
	s_or_b64 exec, exec, s[2:3]
	v_mov_b32_e32 v27, v26
	v_pk_fma_f32 v[18:19], v[144:145], s[50:51], v[8:9] op_sel_hi:[1,0,1]
	v_pk_fma_f32 v[20:21], v[142:143], s[50:51], v[6:7] op_sel_hi:[1,0,1]
	v_mov_b32_e32 v32, v26
	v_mov_b32_e32 v33, v26
	v_pk_mul_f32 v[34:35], v[18:19], v[32:33]
	v_pk_mul_f32 v[18:19], v[20:21], v[26:27]
	v_pk_fma_f32 v[36:37], v[138:139], s[50:51], v[2:3] op_sel_hi:[1,0,1]
	v_med3_f32 v0, v18, s53, v204
	v_pk_mul_f32 v[26:27], v[36:37], v[26:27]
	v_med3_f32 v19, v19, s53, v204
	v_mov_b32_e32 v18, v1
	v_cvt_pk_fp8_f32 v18, v0, v19
	v_med3_f32 v26, v26, s53, v204
	v_med3_f32 v27, v27, s53, v204
	v_mov_b32_e32 v19, v1
	v_cvt_pk_fp8_f32 v19, v26, v27
	v_pk_fma_f32 v[20:21], v[140:141], s[50:51], v[4:5] op_sel_hi:[1,0,1]
	v_med3_f32 v0, v34, s53, v204
	v_pk_mul_f32 v[20:21], v[20:21], v[32:33]
	v_med3_f32 v31, v35, s53, v204
	v_cvt_pk_fp8_f32 v18, v0, v31 op_sel:[0,0,1]
	v_med3_f32 v0, v20, s53, v204
	v_med3_f32 v20, v21, s53, v204
	v_mov_b32_e32 v23, v22
	v_cvt_pk_fp8_f32 v19, v0, v20 op_sel:[0,0,1]
	v_pk_fma_f32 v[20:21], v[136:137], s[50:51], v[8:9] op_sel_hi:[1,0,1]
	v_pk_fma_f32 v[26:27], v[134:135], s[50:51], v[6:7] op_sel_hi:[1,0,1]
	v_mov_b32_e32 v32, v22
	v_mov_b32_e32 v33, v22
	v_pk_mul_f32 v[34:35], v[20:21], v[32:33]
	v_pk_mul_f32 v[20:21], v[26:27], v[22:23]
	v_pk_fma_f32 v[36:37], v[130:131], s[50:51], v[2:3] op_sel_hi:[1,0,1]
	v_med3_f32 v0, v20, s53, v204
	v_pk_mul_f32 v[22:23], v[36:37], v[22:23]
	v_med3_f32 v21, v21, s53, v204
	v_mov_b32_e32 v20, v1
	v_cvt_pk_fp8_f32 v20, v0, v21
	v_med3_f32 v22, v22, s53, v204
	v_med3_f32 v23, v23, s53, v204
	v_mov_b32_e32 v21, v1
	v_cvt_pk_fp8_f32 v21, v22, v23
	v_pk_fma_f32 v[26:27], v[132:133], s[50:51], v[4:5] op_sel_hi:[1,0,1]
	v_med3_f32 v0, v34, s53, v204
	v_pk_mul_f32 v[26:27], v[26:27], v[32:33]
	v_med3_f32 v31, v35, s53, v204
	v_cvt_pk_fp8_f32 v20, v0, v31 op_sel:[0,0,1]
	v_med3_f32 v0, v26, s53, v204
	v_med3_f32 v22, v27, s53, v204
	v_cvt_pk_fp8_f32 v21, v0, v22 op_sel:[0,0,1]
	v_permlane16_swap_b32_e32 v18, v20
	s_nop 0
	v_permlane16_swap_b32_e32 v19, v21
	s_and_saveexec_b64 s[2:3], vcc
	s_cbranch_execz .LBB0_1337
	global_store_dwordx4 v[24:25], v[18:21], off offset:128 nt

; #define LAS __attribute__((address_space(3)))
; DI unsigned pk4_fp8(float a, float b, float c, float d) { int r = 0; r = __builtin_amdgcn_cvt_pk_fp8_f32(sat8(a), sat8(b), r, false); r = __builtin_amdgcn_cvt_pk_fp8_f32(sat8(c), sat8(d), r, true); return (unsigned)r; }
;     DI void operator()(const f32x4 (&acc)[2][2][4][2], const Unit& u, int wr, int wc, int fr, int fq) const {
;     ...
;         for (int ai = 0; ai < 2; ++ai) { if (u.half == 2 - ai) continue;
;             const bool oddq = (fq & 1) != 0;
; #pragma unroll
;             for (int p2 = 0; p2 < 2; ++p2) { u32x2 wq[2][2];
;                 const u32x2 en0 = *(const LAS u32x2*)((const LAS unsigned char*)entl + (128 * ai + 32 * p2 + lrow) * 8), en1 = *(const LAS u32x2*)((const LAS unsigned char*)entl + (128 * ai + 32 * p2 + 16 + lrow) * 8);
; #pragma unroll
;                 for (int r2 = 0; r2 < 2; ++r2) { const int m = 2 * p2 + r2; const float gs = __uint_as_float(r2 ? en1.y : en0.y) * YS8_SCALE;
;                     const f32x4 a0 = (acc[ai][0][m][0] * dq + bv[0][0]) * gs, a1 = (acc[ai][0][m][1] * dq + bv[0][1]) * gs, b0 = (acc[ai][1][m][0] * dq + bv[1][0]) * gs, b1 = (acc[ai][1][m][1] * dq + bv[1][1]) * gs;
;                     wq[r2][0].x = pk4_fp8(a0[0], a0[1], a0[2], a0[3]); wq[r2][0].y = pk4_fp8(a1[0], a1[1], a1[2], a1[3]); wq[r2][1].x = pk4_fp8(b0[0], b0[1], b0[2], b0[3]); wq[r2][1].y = pk4_fp8(b1[0], b1[1], b1[2], b1[3]); }
;                 const int msel = 2 * p2 + (oddq ? 1 : 0); const int li = u.j * 256 + 128 * ai + 16 * msel + lrow;
;                 char* dst = (char*)yslot + ((oddq ? en1.x : en0.x) * (unsigned)D + (unsigned)(cw - (oddq ? 8 : 0)));
; #pragma unroll
;                 for (int bj = 0; bj < 2; ++bj) { const auto rx = __builtin_amdgcn_permlane16_swap(wq[0][bj].x, wq[1][bj].x, false, false), ry = __builtin_amdgcn_permlane16_swap(wq[0][bj].y, wq[1][bj].y, false, false);
;                     u32x4 w; w.x = rx[0]; w.y = ry[0]; w.z = rx[1]; w.w = ry[1];
;                     if (li < n) *(u32x4*)(dst + 128 * bj) = w; } }
.LBB0_1340:
	s_add_i32 s0, 0, 0x20700
	v_add_u32_e32 v30, s0, v30
	s_waitcnt lgkmcnt(0)
	ds_read2_b64 v[32:35], v30 offset0:128 offset1:144
	v_pk_fma_f32 v[18:19], v[128:129], s[50:51], v[16:17] op_sel_hi:[1,0,1]
	v_pk_fma_f32 v[20:21], v[126:127], s[50:51], v[14:15] op_sel_hi:[1,0,1]
	v_pk_fma_f32 v[22:23], v[124:125], s[50:51], v[12:13] op_sel_hi:[1,0,1]
	v_pk_fma_f32 v[38:39], v[114:115], s[50:51], v[10:11] op_sel_hi:[1,0,1]
	s_waitcnt lgkmcnt(0)
	v_mul_f32_e32 v26, 0x42800000, v33
	v_pk_mul_f32 v[24:25], v[18:19], v[26:27] op_sel_hi:[1,0]
	v_pk_mul_f32 v[18:19], v[20:21], v[26:27] op_sel_hi:[1,0]
	v_pk_fma_f32 v[20:21], v[122:123], s[50:51], v[10:11] op_sel_hi:[1,0,1]
	v_med3_f32 v0, v18, s53, v204
	v_pk_mul_f32 v[20:21], v[20:21], v[26:27] op_sel_hi:[1,0]
	v_med3_f32 v19, v19, s53, v204
	v_mov_b32_e32 v18, v1
	v_cvt_pk_fp8_f32 v18, v0, v19
	v_med3_f32 v20, v20, s53, v204
	v_med3_f32 v21, v21, s53, v204
	v_mov_b32_e32 v19, v1
	v_cvt_pk_fp8_f32 v19, v20, v21
	v_pk_mul_f32 v[22:23], v[22:23], v[26:27] op_sel_hi:[1,0]
	v_med3_f32 v0, v24, s53, v204
	v_med3_f32 v24, v25, s53, v204
	v_cvt_pk_fp8_f32 v18, v0, v24 op_sel:[0,0,1]
	v_med3_f32 v0, v22, s53, v204
	v_med3_f32 v20, v23, s53, v204
	v_cvt_pk_fp8_f32 v19, v0, v20 op_sel:[0,0,1]
	v_mul_f32_e32 v22, 0x42800000, v35
	v_pk_fma_f32 v[20:21], v[120:121], s[50:51], v[16:17] op_sel_hi:[1,0,1]
	v_pk_fma_f32 v[24:25], v[118:119], s[50:51], v[14:15] op_sel_hi:[1,0,1]
	v_pk_mul_f32 v[36:37], v[20:21], v[22:23] op_sel_hi:[1,0]
	v_pk_mul_f32 v[20:21], v[24:25], v[22:23] op_sel_hi:[1,0]
	v_pk_mul_f32 v[38:39], v[38:39], v[22:23] op_sel_hi:[1,0]
	v_med3_f32 v0, v20, s53, v204
	v_med3_f32 v21, v21, s53, v204
	v_mov_b32_e32 v20, v1
	v_cvt_pk_fp8_f32 v20, v0, v21
	v_med3_f32 v27, v38, s53, v204
	v_med3_f32 v31, v39, s53, v204
	v_mov_b32_e32 v21, v1
	v_cvt_pk_fp8_f32 v21, v27, v31
	v_pk_fma_f32 v[24:25], v[116:117], s[50:51], v[12:13] op_sel_hi:[1,0,1]
	v_med3_f32 v0, v36, s53, v204
	v_pk_mul_f32 v[24:25], v[24:25], v[22:23] op_sel_hi:[1,0]
	v_med3_f32 v23, v37, s53, v204
	v_cvt_pk_fp8_f32 v20, v0, v23 op_sel:[0,0,1]
	v_med3_f32 v0, v24, s53, v204
	v_med3_f32 v23, v25, s53, v204
	v_cvt_pk_fp8_f32 v21, v0, v23 op_sel:[0,0,1]
	v_cndmask_b32_e64 v0, v34, v32, s[6:7]
	v_add_u32_e32 v23, 0x80, v29
	v_lshl_add_u32 v0, v0, 10, v28
	v_lshl_add_u64 v[24:25], s[10:11], 0, v[0:1]
	v_cmp_gt_i32_e32 vcc, s70, v23
	v_permlane16_swap_b32_e32 v18, v20
	v_permlane16_swap_b32_e32 v19, v21
	s_and_saveexec_b64 s[2:3], vcc
	s_cbranch_execz .LBB0_1342
	global_store_dwordx4 v[24:25], v[18:21], off nt
.LBB0_1342:
	s_or_b64 exec, exec, s[2:3]
	v_mov_b32_e32 v27, v26
	v_pk_fma_f32 v[18:19], v[112:113], s[50:51], v[8:9] op_sel_hi:[1,0,1]
	v_pk_fma_f32 v[20:21], v[110:111], s[50:51], v[6:7] op_sel_hi:[1,0,1]
	v_mov_b32_e32 v32, v26
	v_mov_b32_e32 v33, v26
	v_pk_mul_f32 v[34:35], v[18:19], v[32:33]
	v_pk_mul_f32 v[18:19], v[20:21], v[26:27]
	v_pk_fma_f32 v[36:37], v[106:107], s[50:51], v[2:3] op_sel_hi:[1,0,1]
	v_med3_f32 v0, v18, s53, v204
	v_pk_mul_f32 v[26:27], v[36:37], v[26:27]
	v_med3_f32 v19, v19, s53, v204
	v_mov_b32_e32 v18, v1
	v_cvt_pk_fp8_f32 v18, v0, v19
	v_med3_f32 v26, v26, s53, v204
	v_med3_f32 v27, v27, s53, v204
	v_mov_b32_e32 v19, v1
	v_cvt_pk_fp8_f32 v19, v26, v27
	v_pk_fma_f32 v[20:21], v[108:109], s[50:51], v[4:5] op_sel_hi:[1,0,1]
	v_med3_f32 v0, v34, s53, v204
	v_pk_mul_f32 v[20:21], v[20:21], v[32:33]
	v_med3_f32 v31, v35, s53, v204
	v_cvt_pk_fp8_f32 v18, v0, v31 op_sel:[0,0,1]
	v_med3_f32 v0, v20, s53, v204
	v_med3_f32 v20, v21, s53, v204
	v_mov_b32_e32 v23, v22
	v_cvt_pk_fp8_f32 v19, v0, v20 op_sel:[0,0,1]
	v_pk_fma_f32 v[20:21], v[104:105], s[50:51], v[8:9] op_sel_hi:[1,0,1]
	v_pk_fma_f32 v[26:27], v[102:103], s[50:51], v[6:7] op_sel_hi:[1,0,1]
	v_mov_b32_e32 v32, v22
	v_mov_b32_e32 v33, v22
	v_pk_mul_f32 v[34:35], v[20:21], v[32:33]
	v_pk_mul_f32 v[20:21], v[26:27], v[22:23]
	v_pk_fma_f32 v[36:37], v[98:99], s[50:51], v[2:3] op_sel_hi:[1,0,1]
	v_med3_f32 v0, v20, s53, v204
	v_pk_mul_f32 v[22:23], v[36:37], v[22:23]
	v_med3_f32 v21, v21, s53, v204
	v_mov_b32_e32 v20, v1
	v_cvt_pk_fp8_f32 v20, v0, v21
	v_med3_f32 v22, v22, s53, v204
	v_med3_f32 v23, v23, s53, v204
	v_mov_b32_e32 v21, v1
	v_cvt_pk_fp8_f32 v21, v22, v23
	v_pk_fma_f32 v[26:27], v[100:101], s[50:51], v[4:5] op_sel_hi:[1,0,1]
	v_med3_f32 v0, v34, s53, v204
	v_pk_mul_f32 v[26:27], v[26:27], v[32:33]
	v_med3_f32 v31, v35, s53, v204
	v_cvt_pk_fp8_f32 v20, v0, v31 op_sel:[0,0,1]
	v_med3_f32 v0, v26, s53, v204
	v_med3_f32 v22, v27, s53, v204
	v_cvt_pk_fp8_f32 v21, v0, v22 op_sel:[0,0,1]
	v_permlane16_swap_b32_e32 v18, v20
	s_nop 0
	v_permlane16_swap_b32_e32 v19, v21
	s_and_saveexec_b64 s[2:3], vcc
	s_cbranch_execz .LBB0_1344
	global_store_dwordx4 v[24:25], v[18:21], off offset:128 nt
; #define LAS __attribute__((address_space(3)))
; DI unsigned pk4_fp8(float a, float b, float c, float d) { int r = 0; r = __builtin_amdgcn_cvt_pk_fp8_f32(sat8(a), sat8(b), r, false); r = __builtin_amdgcn_cvt_pk_fp8_f32(sat8(c), sat8(d), r, true); return (unsigned)r; }
;     DI void operator()(const f32x4 (&acc)[2][2][4][2], const Unit& u, int wr, int wc, int fr, int fq) const {
;     ...
;         for (int ai = 0; ai < 2; ++ai) { if (u.half == 2 - ai) continue;
;             const bool oddq = (fq & 1) != 0;
; #pragma unroll
;             for (int p2 = 0; p2 < 2; ++p2) { u32x2 wq[2][2];
;                 const u32x2 en0 = *(const LAS u32x2*)((const LAS unsigned char*)entl + (128 * ai + 32 * p2 + lrow) * 8), en1 = *(const LAS u32x2*)((const LAS unsigned char*)entl + (128 * ai + 32 * p2 + 16 + lrow) * 8);
; #pragma unroll
;                 for (int r2 = 0; r2 < 2; ++r2) { const int m = 2 * p2 + r2; const float gs = __uint_as_float(r2 ? en1.y : en0.y) * YS8_SCALE;
;                     const f32x4 a0 = (acc[ai][0][m][0] * dq + bv[0][0]) * gs, a1 = (acc[ai][0][m][1] * dq + bv[0][1]) * gs, b0 = (acc[ai][1][m][0] * dq + bv[1][0]) * gs, b1 = (acc[ai][1][m][1] * dq + bv[1][1]) * gs;
;                     wq[r2][0].x = pk4_fp8(a0[0], a0[1], a0[2], a0[3]); wq[r2][0].y = pk4_fp8(a1[0], a1[1], a1[2], a1[3]); wq[r2][1].x = pk4_fp8(b0[0], b0[1], b0[2], b0[3]); wq[r2][1].y = pk4_fp8(b1[0], b1[1], b1[2], b1[3]); }
;                 const int msel = 2 * p2 + (oddq ? 1 : 0); const int li = u.j * 256 + 128 * ai + 16 * msel + lrow;
;                 char* dst = (char*)yslot + ((oddq ? en1.x : en0.x) * (unsigned)D + (unsigned)(cw - (oddq ? 8 : 0)));
; #pragma unroll
;                 for (int bj = 0; bj < 2; ++bj) { const auto rx = __builtin_amdgcn_permlane16_swap(wq[0][bj].x, wq[1][bj].x, false, false), ry = __builtin_amdgcn_permlane16_swap(wq[0][bj].y, wq[1][bj].y, false, false);
;                     u32x4 w; w.x = rx[0]; w.y = ry[0]; w.z = rx[1]; w.w = ry[1];
;                     if (li < n) *(u32x4*)(dst + 128 * bj) = w; } }
.LBB0_1344:
	s_or_b64 exec, exec, s[2:3]
	ds_read2_b64 v[30:33], v30 offset0:160 offset1:176
	v_pk_fma_f32 v[18:19], v[96:97], s[50:51], v[16:17] op_sel_hi:[1,0,1]
	v_pk_fma_f32 v[20:21], v[94:95], s[50:51], v[14:15] op_sel_hi:[1,0,1]
	v_pk_fma_f32 v[22:23], v[92:93], s[50:51], v[12:13] op_sel_hi:[1,0,1]
	v_pk_fma_f32 v[14:15], v[86:87], s[50:51], v[14:15] op_sel_hi:[1,0,1]
	s_waitcnt lgkmcnt(0)
	v_mul_f32_e32 v24, 0x42800000, v31
	v_pk_mul_f32 v[26:27], v[18:19], v[24:25] op_sel_hi:[1,0]
	v_pk_mul_f32 v[18:19], v[20:21], v[24:25] op_sel_hi:[1,0]
	v_pk_fma_f32 v[20:21], v[90:91], s[50:51], v[10:11] op_sel_hi:[1,0,1]
	v_med3_f32 v0, v18, s53, v204
	v_med3_f32 v19, v19, s53, v204
	v_mov_b32_e32 v18, v1
	v_pk_mul_f32 v[20:21], v[20:21], v[24:25] op_sel_hi:[1,0]
	v_cvt_pk_fp8_f32 v18, v0, v19
	v_med3_f32 v20, v20, s53, v204
	v_med3_f32 v21, v21, s53, v204
	v_mov_b32_e32 v19, v1
	v_cvt_pk_fp8_f32 v19, v20, v21
	v_pk_mul_f32 v[22:23], v[22:23], v[24:25] op_sel_hi:[1,0]
	v_med3_f32 v0, v26, s53, v204
	v_med3_f32 v25, v27, s53, v204
	v_cvt_pk_fp8_f32 v18, v0, v25 op_sel:[0,0,1]
	v_med3_f32 v0, v22, s53, v204
	v_mul_f32_e32 v22, 0x42800000, v33
	v_med3_f32 v20, v23, s53, v204
	v_pk_mul_f32 v[14:15], v[14:15], v[22:23] op_sel_hi:[1,0]
	v_pk_fma_f32 v[10:11], v[82:83], s[50:51], v[10:11] op_sel_hi:[1,0,1]
	v_cvt_pk_fp8_f32 v19, v0, v20 op_sel:[0,0,1]
	v_pk_mul_f32 v[10:11], v[10:11], v[22:23] op_sel_hi:[1,0]
	v_med3_f32 v0, v14, s53, v204
	v_med3_f32 v14, v15, s53, v204
	v_mov_b32_e32 v20, v1
	v_cvt_pk_fp8_f32 v20, v0, v14
	v_med3_f32 v10, v10, s53, v204
	v_med3_f32 v11, v11, s53, v204
	v_mov_b32_e32 v21, v1
	v_pk_fma_f32 v[16:17], v[88:89], s[50:51], v[16:17] op_sel_hi:[1,0,1]
	v_cvt_pk_fp8_f32 v21, v10, v11
	v_pk_mul_f32 v[16:17], v[16:17], v[22:23] op_sel_hi:[1,0]
	v_pk_fma_f32 v[12:13], v[84:85], s[50:51], v[12:13] op_sel_hi:[1,0,1]
	v_med3_f32 v0, v16, s53, v204
	v_pk_mul_f32 v[12:13], v[12:13], v[22:23] op_sel_hi:[1,0]
	v_med3_f32 v14, v17, s53, v204
	v_cvt_pk_fp8_f32 v20, v0, v14 op_sel:[0,0,1]
	v_med3_f32 v0, v12, s53, v204
	v_med3_f32 v10, v13, s53, v204
	v_cvt_pk_fp8_f32 v21, v0, v10 op_sel:[0,0,1]
	v_cndmask_b32_e64 v0, v32, v30, s[6:7]
	v_add_u32_e32 v10, 0xa0, v29
	v_lshl_add_u32 v0, v0, 10, v28
	v_lshl_add_u64 v[14:15], s[10:11], 0, v[0:1]
	v_cmp_gt_i32_e32 vcc, s70, v10
	v_permlane16_swap_b32_e32 v18, v20
	v_permlane16_swap_b32_e32 v19, v21
	s_and_saveexec_b64 s[2:3], vcc
	s_cbranch_execz .LBB0_1346
	global_store_dwordx4 v[14:15], v[18:21], off nt
.LBB0_1346:
	s_or_b64 exec, exec, s[2:3]
	v_mov_b32_e32 v25, v24
	v_pk_fma_f32 v[10:11], v[80:81], s[50:51], v[8:9] op_sel_hi:[1,0,1]
	v_pk_fma_f32 v[12:13], v[78:79], s[50:51], v[6:7] op_sel_hi:[1,0,1]
	v_mov_b32_e32 v16, v24
	v_mov_b32_e32 v17, v24
	v_pk_mul_f32 v[18:19], v[10:11], v[16:17]
	v_pk_mul_f32 v[10:11], v[12:13], v[24:25]
	v_pk_fma_f32 v[12:13], v[76:77], s[50:51], v[4:5] op_sel_hi:[1,0,1]
	v_pk_fma_f32 v[20:21], v[74:75], s[50:51], v[2:3] op_sel_hi:[1,0,1]
	v_pk_mul_f32 v[12:13], v[12:13], v[16:17]
	v_pk_mul_f32 v[16:17], v[20:21], v[24:25]
	v_med3_f32 v0, v10, s53, v204
	v_med3_f32 v11, v11, s53, v204
	v_mov_b32_e32 v10, v1
	v_cvt_pk_fp8_f32 v10, v0, v11
	v_med3_f32 v16, v16, s53, v204
	v_med3_f32 v17, v17, s53, v204
	v_mov_b32_e32 v11, v1
	v_cvt_pk_fp8_f32 v11, v16, v17
	v_med3_f32 v0, v18, s53, v204
	v_med3_f32 v18, v19, s53, v204
	v_mov_b32_e32 v23, v22
	v_cvt_pk_fp8_f32 v10, v0, v18 op_sel:[0,0,1]
	v_med3_f32 v0, v12, s53, v204
	v_med3_f32 v12, v13, s53, v204
	v_pk_fma_f32 v[6:7], v[70:71], s[50:51], v[6:7] op_sel_hi:[1,0,1]
	v_cvt_pk_fp8_f32 v11, v0, v12 op_sel:[0,0,1]
	v_pk_fma_f32 v[8:9], v[72:73], s[50:51], v[8:9] op_sel_hi:[1,0,1]
	v_mov_b32_e32 v12, v22
	v_mov_b32_e32 v13, v22
	v_pk_mul_f32 v[6:7], v[6:7], v[22:23]
	v_pk_fma_f32 v[4:5], v[68:69], s[50:51], v[4:5] op_sel_hi:[1,0,1]
	v_pk_fma_f32 v[2:3], v[66:67], s[50:51], v[2:3] op_sel_hi:[1,0,1]
	v_pk_mul_f32 v[8:9], v[8:9], v[12:13]
	v_pk_mul_f32 v[4:5], v[4:5], v[12:13]
	v_pk_mul_f32 v[2:3], v[2:3], v[22:23]
	v_med3_f32 v0, v6, s53, v204
	v_med3_f32 v6, v7, s53, v204
	v_mov_b32_e32 v12, v1
	v_cvt_pk_fp8_f32 v12, v0, v6
	v_med3_f32 v2, v2, s53, v204
	v_med3_f32 v3, v3, s53, v204
	v_mov_b32_e32 v13, v1
	v_cvt_pk_fp8_f32 v13, v2, v3
	v_med3_f32 v0, v8, s53, v204
	v_med3_f32 v6, v9, s53, v204
	v_cvt_pk_fp8_f32 v12, v0, v6 op_sel:[0,0,1]
	v_med3_f32 v0, v4, s53, v204
	v_med3_f32 v2, v5, s53, v204
	v_cvt_pk_fp8_f32 v13, v0, v2 op_sel:[0,0,1]
	v_permlane16_swap_b32_e32 v10, v12
	s_nop 0
	v_permlane16_swap_b32_e32 v11, v13
	s_and_saveexec_b64 s[2:3], vcc
	s_cbranch_execz .LBB0_1348
	global_store_dwordx4 v[14:15], v[10:13], off offset:128 nt
